# attention PV segment: counted lgkmcnt waits per MFMA instead of lgkmcnt(0) before the fourth MFMA of each group; stacked on combined version
# baseline (speedup 1.0000x reference)
.LBB0_1168:
	s_nop 8
	v_exp_f32_e32 v1, v82
	s_nop 0
	v_exp_f32_e32 v66, v66
	v_exp_f32_e32 v82, v83
	v_exp_f32_e32 v69, v69
	v_add_f32_e32 v1, 1.0, v1
	v_add_f32_e32 v83, 1.0, v66
	v_rcp_f32_e32 v66, v1
	v_exp_f32_e32 v1, v67
	v_add_f32_e32 v67, 1.0, v82
	v_exp_f32_e32 v82, v84
	v_exp_f32_e32 v84, v70
	v_add_f32_e32 v69, 1.0, v69
	v_rcp_f32_e32 v204, v69
	v_exp_f32_e32 v69, v86
	v_add_f32_e32 v84, 1.0, v84
	v_rcp_f32_e32 v210, v84
	v_exp_f32_e32 v84, v71
	v_exp_f32_e32 v73, v73
	v_exp_f32_e32 v77, v77
	v_exp_f32_e32 v80, v80
	v_add_f32_e32 v84, 1.0, v84
	v_rcp_f32_e32 v211, v84
	v_exp_f32_e32 v84, v89
	v_add_f32_e32 v73, 1.0, v73
	v_rcp_f32_e32 v212, v73
	v_exp_f32_e32 v73, v90
	v_add_f32_e32 v84, 1.0, v84
	v_rcp_f32_e32 v86, v84
	v_exp_f32_e32 v84, v74
	v_add_f32_e32 v73, 1.0, v73
	v_rcp_f32_e32 v74, v73
	v_exp_f32_e32 v73, v91
	v_add_f32_e32 v84, 1.0, v84
	v_rcp_f32_e32 v90, v84
	v_exp_f32_e32 v84, v75
	v_add_f32_e32 v73, 1.0, v73
	v_rcp_f32_e32 v75, v73
	v_exp_f32_e32 v73, v92
	v_add_f32_e32 v84, 1.0, v84
	v_rcp_f32_e32 v91, v84
	v_exp_f32_e32 v84, v93
	v_add_f32_e32 v77, 1.0, v77
	v_exp_f32_e32 v81, v81
	v_rcp_f32_e32 v220, v77
	v_add_f32_e32 v84, 1.0, v84
	v_rcp_f32_e32 v92, v84
	v_exp_f32_e32 v84, v78
	v_exp_f32_e32 v77, v94
	v_add_f32_e32 v69, 1.0, v69
	v_rcp_f32_e32 v70, v69
	v_add_f32_e32 v84, 1.0, v84
	v_rcp_f32_e32 v94, v84
	v_exp_f32_e32 v84, v79
	v_exp_f32_e32 v69, v87
	v_exp_f32_e32 v76, v76
	v_add_f32_e32 v80, 1.0, v80
	v_add_f32_e32 v81, 1.0, v81
	v_add_f32_e32 v77, 1.0, v77
	v_add_f32_e32 v84, 1.0, v84
	v_rcp_f32_e32 v93, v80
	v_rcp_f32_e32 v170, v81
	v_rcp_f32_e32 v78, v77
	v_exp_f32_e32 v77, v95
	v_rcp_f32_e32 v95, v84
	v_add_f32_e32 v69, 1.0, v69
	v_add_f32_e32 v76, 1.0, v76
	v_exp_f32_e32 v84, v97
	v_rcp_f32_e32 v71, v69
	v_exp_f32_e32 v69, v88
	v_rcp_f32_e32 v88, v76
	v_mul_f32_e32 v237, v93, v170
	v_mul_f32_e32 v236, v95, v237
	v_exp_f32_e32 v72, v72
	v_mul_f32_e32 v81, v94, v236
	v_add_f32_e32 v80, 1.0, v84
	v_pk_add_f32 v[234:235], v[94:95], 1.0 op_sel_hi:[1,0] neg_lo:[1,0] neg_hi:[1,0]
	v_mov_b32_e32 v84, v81
	v_pk_mul_f32 v[234:235], v[234:235], v[236:237]
	s_nop 0
	v_permlane32_swap_b32_e32 v81, v84
	v_mul_f32_e32 v237, v88, v220
	v_sub_f32_e32 v228, 1.0, v93
	v_fma_f32 v229, v176, v84, v190
	v_mul_f32_e32 v236, v91, v237
	v_add_f32_e32 v72, 1.0, v72
	v_sub_f32_e32 v233, 1.0, v170
	v_pk_mul_f32 v[228:229], v[170:171], v[228:229]
	v_mul_f32_e32 v170, v90, v236
	v_rcp_f32_e32 v87, v72
	v_mov_b32_e32 v94, v170
	v_mul_f32_e32 v95, v81, v84
	v_mov_b32_e32 v232, v229
	v_permlane32_swap_b32_e32 v170, v94
	v_pk_mul_f32 v[234:235], v[234:235], v[228:229] op_sel:[0,1]
	v_pk_mul_f32 v[228:229], v[228:229], v[232:233]
	v_pk_add_f32 v[232:233], v[90:91], 1.0 op_sel_hi:[1,0] neg_lo:[1,0] neg_hi:[1,0]
	v_pk_mul_f32 v[90:91], v[170:171], v[94:95]
	v_exp_f32_e32 v68, v68
	v_sub_f32_e32 v222, 1.0, v88
	v_fma_f32 v223, v176, v94, v190
	v_mov_b32_e32 v221, v91
	v_pk_mul_f32 v[94:95], v[220:221], v[222:223]
	v_mul_f32_e32 v223, v87, v212
	v_mul_f32_e32 v222, v211, v223
	v_mul_f32_e32 v81, v210, v222
	v_add_f32_e32 v68, 1.0, v68
	v_mov_b32_e32 v84, v81
	v_rcp_f32_e32 v202, v83
	v_add_f32_e32 v1, 1.0, v1
	v_rcp_f32_e32 v83, v68
	v_pk_mul_f32 v[90:91], v[90:91], v[90:91] op_sel:[0,1] op_sel_hi:[1,0]
	v_permlane32_swap_b32_e32 v81, v84
	v_rcp_f32_e32 v203, v1
	v_sub_f32_e32 v214, 1.0, v87
	v_add_f32_e32 v77, 1.0, v77
	v_mov_b32_e32 v215, v90
	v_fma_f32 v213, v176, v84, v190
	v_sub_f32_e32 v217, 1.0, v212
	v_rcp_f32_e32 v79, v77
	v_exp_f32_e32 v77, v96
	v_pk_add_f32 v[170:171], v[210:211], 1.0 op_sel_hi:[1,0] neg_lo:[1,0] neg_hi:[1,0]
	v_pk_mul_f32 v[212:213], v[212:213], v[214:215]
	v_pk_mul_f32 v[170:171], v[170:171], v[222:223]
	v_mov_b32_e32 v216, v213
	v_pk_mul_f32 v[214:215], v[170:171], v[212:213] op_sel:[0,1]
	v_pk_mul_f32 v[212:213], v[212:213], v[216:217]
	v_mul_f32_e32 v217, v83, v204
	v_mul_f32_e32 v216, v203, v217
	v_add_f32_e32 v77, 1.0, v77
	v_mul_f32_e32 v210, v202, v216
	v_rcp_f32_e32 v77, v77
	v_rcp_f32_e32 v80, v80
	v_pk_add_f32 v[170:171], v[202:203], 1.0 op_sel_hi:[1,0] neg_lo:[1,0] neg_hi:[1,0]
	v_mov_b32_e32 v202, v210
	v_mul_f32_e32 v211, v81, v84
	s_nop 0
	v_permlane32_swap_b32_e32 v210, v202
	v_mov_b32_e32 v203, v90
	v_pk_mul_f32 v[90:91], v[210:211], v[202:203]
	v_sub_f32_e32 v206, 1.0, v83
	v_add_f32_e32 v73, 1.0, v73
	v_fma_f32 v207, v176, v202, v190
	v_mov_b32_e32 v205, v91
	v_rcp_f32_e32 v73, v73
	v_pk_mul_f32 v[202:203], v[204:205], v[206:207]
	v_mul_f32_e32 v207, v77, v80
	v_mul_f32_e32 v206, v79, v207
	v_sub_f32_e32 v96, 1.0, v77
	v_pk_mul_f32 v[170:171], v[170:171], v[216:217]
	v_mul_f32_e32 v77, v78, v206
	v_sub_f32_e32 v209, 1.0, v204
	v_pk_mul_f32 v[204:205], v[170:171], v[202:203] op_sel:[0,1]
	v_pk_add_f32 v[170:171], v[78:79], 1.0 op_sel_hi:[1,0] neg_lo:[1,0] neg_hi:[1,0]
	v_mov_b32_e32 v78, v77
	v_pk_mul_f32 v[90:91], v[90:91], v[90:91] op_sel:[0,1] op_sel_hi:[1,0]
	v_pk_mul_f32 v[170:171], v[170:171], v[206:207]
	v_permlane32_swap_b32_e32 v77, v78
	v_mul_f32_e32 v207, v73, v92
	v_mov_b32_e32 v97, v90
	v_fma_f32 v81, v176, v78, v190
	v_mul_f32_e32 v206, v75, v207
	v_add_f32_e32 v69, 1.0, v69
	v_sub_f32_e32 v231, 1.0, v80
	v_mul_f32_e32 v79, v77, v78
	v_pk_mul_f32 v[80:81], v[80:81], v[96:97]
	v_mul_f32_e32 v78, v74, v206
	v_rcp_f32_e32 v69, v69
	v_pk_mul_f32 v[96:97], v[170:171], v[80:81] op_sel:[0,1]
	v_pk_add_f32 v[170:171], v[74:75], 1.0 op_sel_hi:[1,0] neg_lo:[1,0] neg_hi:[1,0]
	v_mov_b32_e32 v74, v78
	s_nop 1
	v_permlane32_swap_b32_e32 v78, v74
	v_mov_b32_e32 v75, v90
	v_add_f32_e32 v1, 1.0, v82
	v_exp_f32_e32 v82, v85
	v_fma_f32 v77, v176, v74, v190
	v_pk_mul_f32 v[74:75], v[78:79], v[74:75]
	v_sub_f32_e32 v76, 1.0, v73
	v_mov_b32_e32 v93, v75
	v_pk_mul_f32 v[76:77], v[92:93], v[76:77]
	v_mul_f32_e32 v93, v69, v86
	v_sub_f32_e32 v225, 1.0, v92
	v_mul_f32_e32 v92, v71, v93
	v_add_f32_e32 v82, 1.0, v82
	v_sub_f32_e32 v72, 1.0, v69
	v_mul_f32_e32 v69, v70, v92
	v_rcp_f32_e32 v1, v1
	v_rcp_f32_e32 v82, v82
	v_pk_add_f32 v[90:91], v[70:71], 1.0 op_sel_hi:[1,0] neg_lo:[1,0] neg_hi:[1,0]
	v_mov_b32_e32 v70, v69
	v_rcp_f32_e32 v67, v67
	v_pk_mul_f32 v[74:75], v[74:75], v[74:75] op_sel:[0,1] op_sel_hi:[1,0]
	v_permlane32_swap_b32_e32 v69, v70
	v_mov_b32_e32 v73, v74
	v_fma_f32 v87, v176, v70, v190
	v_pk_mul_f32 v[90:91], v[90:91], v[92:93]
	v_pk_mul_f32 v[72:73], v[86:87], v[72:73]
	v_sub_f32_e32 v89, 1.0, v86
	v_pk_mul_f32 v[86:87], v[90:91], v[72:73] op_sel:[0,1]
	v_mul_f32_e32 v91, v1, v82
	v_mul_f32_e32 v90, v67, v91
	v_mul_f32_e32 v71, v69, v70
	v_mov_b32_e32 v88, v73
	v_mul_f32_e32 v70, v66, v90
	v_pk_mul_f32 v[72:73], v[72:73], v[88:89]
	v_pk_add_f32 v[88:89], v[66:67], 1.0 op_sel_hi:[1,0] neg_lo:[1,0] neg_hi:[1,0]
	v_mov_b32_e32 v66, v70
	s_nop 1
	v_permlane32_swap_b32_e32 v70, v66
	v_mov_b32_e32 v67, v74
	v_fma_f32 v69, v176, v66, v190
	v_pk_mul_f32 v[66:67], v[70:71], v[66:67]
	v_sub_f32_e32 v68, 1.0, v1
	v_mov_b32_e32 v83, v67
	v_pk_mul_f32 v[68:69], v[82:83], v[68:69]
	v_sub_f32_e32 v85, 1.0, v82
	v_pk_mul_f32 v[88:89], v[88:89], v[90:91]
	v_mov_b32_e32 v84, v69
	v_add_u32_e32 v1, s61, v191
	ds_read_b64_tr_b16 v[82:83], v1 offset:0
	v_pk_mul_f32 v[170:171], v[170:171], v[206:207]
	v_pk_mul_f32 v[70:71], v[88:89], v[68:69] op_sel:[0,1]
	v_pk_mul_f32 v[68:69], v[68:69], v[84:85]
	ds_read_b64_tr_b16 v[84:85], v1 offset:0x800
	v_pk_mul_f32 v[78:79], v[170:171], v[76:77] op_sel:[0,1]
	v_mul_f32_e32 v171, v66, v67
	v_cvt_pk_bf16_f32 v67, v68, v69
	v_cvt_pk_bf16_f32 v68, v86, v87
	ds_read_b64_tr_b16 v[86:87], v1 offset:0x1000
	ds_read_b64_tr_b16 v[88:89], v1 offset:0x1800
	v_sub_f32_e32 v227, 1.0, v220
	v_pk_mul_f32 v[232:233], v[232:233], v[236:237]
	v_mov_b32_e32 v226, v95
	ds_read_b64_tr_b16 v[90:91], v1 offset:0x2000
	v_pk_mul_f32 v[220:221], v[232:233], v[94:95] op_sel:[0,1]
	v_pk_mul_f32 v[94:95], v[94:95], v[226:227]
	ds_read_b64_tr_b16 v[92:93], v1 offset:0x2800
	v_cvt_pk_bf16_f32 v66, v70, v71
	v_cvt_pk_bf16_f32 v70, v78, v79
	v_cvt_pk_bf16_f32 v79, v94, v95
	ds_read_b64_tr_b16 v[94:95], v1 offset:0x3000
	v_cvt_pk_bf16_f32 v69, v72, v73
	v_cvt_pk_bf16_f32 v72, v96, v97
	ds_read_b64_tr_b16 v[96:97], v1 offset:0x3800
	v_mov_b32_e32 v208, v203
	v_mov_b32_e32 v230, v81
	v_mov_b32_e32 v224, v77
	s_waitcnt lgkmcnt(0)
	v_pk_mul_f32 v[202:203], v[202:203], v[208:209]
	v_pk_mul_f32 v[80:81], v[80:81], v[230:231]
	v_pk_mul_f32 v[76:77], v[76:77], v[224:225]
	v_cvt_pk_bf16_f32 v73, v80, v81
	v_cvt_pk_bf16_f32 v71, v76, v77
	v_cvt_pk_bf16_f32 v74, v204, v205
	v_cvt_pk_bf16_f32 v75, v202, v203
	v_cvt_pk_bf16_f32 v76, v214, v215
	v_cvt_pk_bf16_f32 v77, v212, v213
	v_cvt_pk_bf16_f32 v78, v220, v221
	v_cvt_pk_bf16_f32 v80, v234, v235
	v_cvt_pk_bf16_f32 v81, v228, v229
	v_permlane32_swap_b32_e32 v66, v68
	v_permlane32_swap_b32_e32 v67, v69
	v_permlane32_swap_b32_e32 v70, v72
	v_permlane32_swap_b32_e32 v71, v73
	v_permlane32_swap_b32_e32 v74, v76
	v_permlane32_swap_b32_e32 v75, v77
	v_permlane32_swap_b32_e32 v78, v80
	v_permlane32_swap_b32_e32 v79, v81
	v_mfma_f32_32x32x16_bf16 v[50:65], v[66:69], v[82:85], v[50:65]
	ds_read_b64_tr_b16 v[82:83], v1 offset:0x200
	ds_read_b64_tr_b16 v[84:85], v1 offset:0xa00
	v_mfma_f32_32x32x16_bf16 v[50:65], v[70:73], v[86:89], v[50:65]
	ds_read_b64_tr_b16 v[86:87], v1 offset:0x1200
	ds_read_b64_tr_b16 v[88:89], v1 offset:0x1a00
	v_mfma_f32_32x32x16_bf16 v[50:65], v[74:77], v[90:93], v[50:65]
	ds_read_b64_tr_b16 v[90:91], v1 offset:0x2200
	ds_read_b64_tr_b16 v[92:93], v1 offset:0x2a00
	ds_read_b64_tr_b16 v[202:203], v1 offset:0x3200
	ds_read_b64_tr_b16 v[204:205], v1 offset:0x3a00
	s_nop 0
	v_mfma_f32_32x32x16_bf16 v[50:65], v[78:81], v[94:97], v[50:65]
	s_waitcnt lgkmcnt(6)
	v_mfma_f32_32x32x16_bf16 v[34:49], v[66:69], v[82:85], v[34:49]
	ds_read_b64_tr_b16 v[82:83], v1 offset:0x400
	ds_read_b64_tr_b16 v[84:85], v1 offset:0xc00
	s_waitcnt lgkmcnt(6)
	v_mfma_f32_32x32x16_bf16 v[34:49], v[70:73], v[86:89], v[34:49]
	ds_read_b64_tr_b16 v[86:87], v1 offset:0x1400
	ds_read_b64_tr_b16 v[88:89], v1 offset:0x1c00
	s_waitcnt lgkmcnt(6)
	v_mfma_f32_32x32x16_bf16 v[34:49], v[74:77], v[90:93], v[34:49]
	ds_read_b64_tr_b16 v[90:91], v1 offset:0x2400
	ds_read_b64_tr_b16 v[92:93], v1 offset:0x2c00
	ds_read_b64_tr_b16 v[94:95], v1 offset:0x3400
	ds_read_b64_tr_b16 v[96:97], v1 offset:0x3c00
	s_nop 0
	s_waitcnt lgkmcnt(8)
	v_mfma_f32_32x32x16_bf16 v[34:49], v[78:81], v[202:205], v[34:49]
	s_waitcnt lgkmcnt(6)
	v_mfma_f32_32x32x16_bf16 v[18:33], v[66:69], v[82:85], v[18:33]
	ds_read_b64_tr_b16 v[82:83], v1 offset:0x600
	ds_read_b64_tr_b16 v[84:85], v1 offset:0xe00
	s_waitcnt lgkmcnt(6)
	v_mfma_f32_32x32x16_bf16 v[18:33], v[70:73], v[86:89], v[18:33]
	ds_read_b64_tr_b16 v[86:87], v1 offset:0x1600
	ds_read_b64_tr_b16 v[88:89], v1 offset:0x1e00
	s_waitcnt lgkmcnt(6)
	v_mfma_f32_32x32x16_bf16 v[18:33], v[74:77], v[90:93], v[18:33]
	ds_read_b64_tr_b16 v[90:91], v1 offset:0x2600
	ds_read_b64_tr_b16 v[92:93], v1 offset:0x2e00
	ds_read_b64_tr_b16 v[202:203], v1 offset:0x3600
	ds_read_b64_tr_b16 v[204:205], v1 offset:0x3e00
	s_nop 0
	s_waitcnt lgkmcnt(8)
	v_mfma_f32_32x32x16_bf16 v[18:33], v[78:81], v[94:97], v[18:33]
	s_waitcnt lgkmcnt(6)
	v_mfma_f32_32x32x16_bf16 v[2:17], v[66:69], v[82:85], v[2:17]
	s_waitcnt lgkmcnt(4)
	v_mfma_f32_32x32x16_bf16 v[2:17], v[70:73], v[86:89], v[2:17]
	s_waitcnt lgkmcnt(2)
	v_mfma_f32_32x32x16_bf16 v[2:17], v[74:77], v[90:93], v[2:17]
	s_waitcnt lgkmcnt(0)
	v_mfma_f32_32x32x16_bf16 v[2:17], v[78:81], v[202:205], v[2:17]
